# gemm1/gemm2 unit switch (MoeOrder::next): expert table read in one LDS batch and counted arithmetically instead of 8 serialized read->wait->compare steps
# speedup vs baseline: 1.0086x; 1.0041x over previous
;     __device__ bool next(int i, Unit& u) const {
;         const long L0 = (long)i * G + c; const int ntile = tab[16], nwg = ntile * nN;
;         if (L0 >= (long)nwg) return false;
;         int L = (int)L0; { const int q = nwg / NXCD, r = nwg % NXCD, xcd = L % NXCD, off = L / NXCD; L = (xcd < r ? xcd * (q + 1) : r * (q + 1) + (xcd - r) * q) + off; }
;         const int tile = L / nN; u.pn = L % nN;
;         int e = 0;
; #pragma unroll
;         for (int k = 1; k < 16; ++k) e += (tab[k] <= tile) ? 1 : 0;
;         u.e = e; u.row0 = tab[17 + e] + (tile - tab[e]) * BM; u.rend = tab[17 + e + 1]; u.koff = 0; u.kt = K / BK; u.loff = e * T - tab[17 + e]; return true;
.LBB0_1207:
	s_ashr_i32 s4, s22, 3
	s_add_i32 s5, s27, s4
	s_ashr_i32 s4, s5, 31
	s_lshr_b32 s4, s4, 30
	s_add_i32 s22, s5, s4
	s_ashr_i32 s4, s22, 2
	s_and_b32 s22, s22, -4
	s_sub_i32 s22, s5, s22
	v_mov_b32_e32 v4, 0x20004
	ds_read2_b32 v[8:9], v4 offset1:1
	ds_read2_b32 v[10:11], v4 offset0:2 offset1:3
	ds_read2_b32 v[12:13], v4 offset0:4 offset1:5
	ds_read2_b32 v[14:15], v4 offset0:6 offset1:7
	ds_read2_b32 v[16:17], v4 offset0:8 offset1:9
	ds_read2_b32 v[18:19], v4 offset0:10 offset1:11
	ds_read2_b32 v[20:21], v4 offset0:12 offset1:13
	ds_read_b32 v22, v4 offset:56
	s_waitcnt lgkmcnt(0)
	v_sub_u32_e32 v8, s4, v8
	v_sub_u32_e32 v9, s4, v9
	v_sub_u32_e32 v10, s4, v10
	v_sub_u32_e32 v11, s4, v11
	v_sub_u32_e32 v12, s4, v12
	v_sub_u32_e32 v13, s4, v13
	v_sub_u32_e32 v14, s4, v14
	v_sub_u32_e32 v15, s4, v15
	v_sub_u32_e32 v16, s4, v16
	v_sub_u32_e32 v17, s4, v17
	v_sub_u32_e32 v18, s4, v18
	v_sub_u32_e32 v19, s4, v19
	v_sub_u32_e32 v20, s4, v20
	v_sub_u32_e32 v21, s4, v21
	v_sub_u32_e32 v22, s4, v22
	v_lshrrev_b32_e32 v8, 31, v8
	v_lshrrev_b32_e32 v9, 31, v9
	v_lshrrev_b32_e32 v10, 31, v10
	v_lshrrev_b32_e32 v11, 31, v11
	v_lshrrev_b32_e32 v12, 31, v12
	v_lshrrev_b32_e32 v13, 31, v13
	v_lshrrev_b32_e32 v14, 31, v14
	v_lshrrev_b32_e32 v15, 31, v15
	v_lshrrev_b32_e32 v16, 31, v16
	v_lshrrev_b32_e32 v17, 31, v17
	v_lshrrev_b32_e32 v18, 31, v18
	v_lshrrev_b32_e32 v19, 31, v19
	v_lshrrev_b32_e32 v20, 31, v20
	v_lshrrev_b32_e32 v21, 31, v21
	v_lshrrev_b32_e32 v22, 31, v22
	v_add3_u32 v8, v8, v9, v10
	v_add3_u32 v11, v11, v12, v13
	v_add3_u32 v14, v14, v15, v16
	v_add3_u32 v17, v17, v18, v19
	v_add3_u32 v20, v20, v21, v22
	v_add3_u32 v8, v8, v11, v14
	v_add3_u32 v8, v8, v17, v20
	v_sub_u32_e32 v190, 15, v8
	v_lshlrev_b32_e32 v4, 2, v190
	v_add_u32_e32 v4, 0, v4
	v_add_u32_e32 v4, 0x20000, v4
	ds_read2_b32 v[192:193], v4 offset0:17 offset1:18
	ds_read_b32 v4, v4
	s_waitcnt lgkmcnt(0)
	v_sub_u32_e32 v4, s4, v4
	v_lshlrev_b32_e32 v4, 8, v4
	s_mov_b32 s4, 0x8080
	v_add_u32_e32 v227, v4, v192
	v_mul_lo_u32 v4, v190, s4
	v_sub_u32_e32 v192, v4, v192

;     __device__ bool next(int i, Unit& u) const {
;         const long L0 = (long)i * G + c; const int ntile = tab[16], nwg = ntile * nN;
;         if (L0 >= (long)nwg) return false;
;         int L = (int)L0; { const int q = nwg / NXCD, r = nwg % NXCD, xcd = L % NXCD, off = L / NXCD; L = (xcd < r ? xcd * (q + 1) : r * (q + 1) + (xcd - r) * q) + off; }
;         const int tile = L / nN; u.pn = L % nN;
;         int e = 0;
; #pragma unroll
;         for (int k = 1; k < 16; ++k) e += (tab[k] <= tile) ? 1 : 0;
;         u.e = e; u.row0 = tab[17 + e] + (tile - tab[e]) * BM; u.rend = tab[17 + e + 1]; u.koff = 0; u.kt = K / BK; u.loff = e * T - tab[17 + e]; return true;
.LBB0_1474:
	s_ashr_i32 s4, s24, 3
	s_add_i32 s5, s27, s4
	s_ashr_i32 s4, s5, 31
	s_lshr_b32 s4, s4, 30
	s_add_i32 s24, s5, s4
	s_ashr_i32 s4, s24, 2
	s_and_b32 s24, s24, -4
	s_sub_i32 s24, s5, s24
	v_mov_b32_e32 v4, 0x20004
	ds_read2_b32 v[8:9], v4 offset1:1
	ds_read2_b32 v[10:11], v4 offset0:2 offset1:3
	ds_read2_b32 v[12:13], v4 offset0:4 offset1:5
	ds_read2_b32 v[14:15], v4 offset0:6 offset1:7
	ds_read2_b32 v[16:17], v4 offset0:8 offset1:9
	ds_read2_b32 v[18:19], v4 offset0:10 offset1:11
	ds_read2_b32 v[20:21], v4 offset0:12 offset1:13
	ds_read_b32 v22, v4 offset:56
	s_waitcnt lgkmcnt(0)
	v_sub_u32_e32 v8, s4, v8
	v_sub_u32_e32 v9, s4, v9
	v_sub_u32_e32 v10, s4, v10
	v_sub_u32_e32 v11, s4, v11
	v_sub_u32_e32 v12, s4, v12
	v_sub_u32_e32 v13, s4, v13
	v_sub_u32_e32 v14, s4, v14
	v_sub_u32_e32 v15, s4, v15
	v_sub_u32_e32 v16, s4, v16
	v_sub_u32_e32 v17, s4, v17
	v_sub_u32_e32 v18, s4, v18
	v_sub_u32_e32 v19, s4, v19
	v_sub_u32_e32 v20, s4, v20
	v_sub_u32_e32 v21, s4, v21
	v_sub_u32_e32 v22, s4, v22
	v_lshrrev_b32_e32 v8, 31, v8
	v_lshrrev_b32_e32 v9, 31, v9
	v_lshrrev_b32_e32 v10, 31, v10
	v_lshrrev_b32_e32 v11, 31, v11
	v_lshrrev_b32_e32 v12, 31, v12
	v_lshrrev_b32_e32 v13, 31, v13
	v_lshrrev_b32_e32 v14, 31, v14
	v_lshrrev_b32_e32 v15, 31, v15
	v_lshrrev_b32_e32 v16, 31, v16
	v_lshrrev_b32_e32 v17, 31, v17
	v_lshrrev_b32_e32 v18, 31, v18
	v_lshrrev_b32_e32 v19, 31, v19
	v_lshrrev_b32_e32 v20, 31, v20
	v_lshrrev_b32_e32 v21, 31, v21
	v_lshrrev_b32_e32 v22, 31, v22
	v_add3_u32 v8, v8, v9, v10
	v_add3_u32 v11, v11, v12, v13
	v_add3_u32 v14, v14, v15, v16
	v_add3_u32 v17, v17, v18, v19
	v_add3_u32 v20, v20, v21, v22
	v_add3_u32 v8, v8, v11, v14
	v_add3_u32 v8, v8, v17, v20
	v_sub_u32_e32 v190, 15, v8
	v_lshlrev_b32_e32 v4, 2, v190
	v_add_u32_e32 v4, 0, v4
	v_add_u32_e32 v4, 0x20000, v4
	ds_read2_b32 v[192:193], v4 offset0:17 offset1:18
	ds_read_b32 v4, v4
	s_waitcnt lgkmcnt(0)
	v_sub_u32_e32 v4, s4, v4
	v_lshlrev_b32_e32 v4, 8, v4
	s_mov_b32 s4, 0x8080
	v_add_u32_e32 v228, v4, v192
	v_mul_lo_u32 v4, v190, s4
	v_sub_u32_e32 v192, v4, v192
